# speedup vs baseline: 1.0448x; 1.0125x over previous
_Z6k_prepPKfS0_S0_S0_PDF16_S1_S1_S1_S0_S0_S0_:
	s_load_dwordx2 s[8:9], s[0:1], 0x8
	v_and_b32_e32 v1, 31, v0
	s_cmpk_lt_i32 s2, 0x100
	s_cbranch_scc1 .Lp_main
	s_cmpk_lt_i32 s2, 0x140
	s_cbranch_scc0 .Lp_w1t
	s_endpgm
.Lp_main:
	s_load_dwordx2 s[10:11], s[0:1], 0x0
	s_load_dwordx4 s[12:15], s[0:1], 0x10
	s_load_dwordx2 s[16:17], s[0:1], 0x20
	s_load_dwordx4 s[20:23], s[0:1], 0x28
	v_readfirstlane_b32 s3, v0
	v_and_b32_e32 v154, 63, v0
	v_lshrrev_b32_e32 v155, 5, v154
	v_lshlrev_b32_e32 v156, 4, v0
	v_lshlrev_b32_e32 v157, 4, v154
	v_lshlrev_b32_e32 v158, 8, v1
	v_lshl_add_u32 v158, v155, 5, v158
	v_lshlrev_b32_e32 v159, 4, v155
	v_lshrrev_b32_e32 v160, 3, v0
	v_lshlrev_b32_e32 v160, 12, v160
	v_and_b32_e32 v161, 7, v0
	v_lshl_add_u32 v160, v161, 4, v160
	s_lshr_b32 s24, s2, 3
	s_and_b32 s25, s2, 7
	s_lshr_b32 s26, s3, 6
	s_lshl_b32 s27, s25, 2
	s_add_u32 s27, s27, s26
	s_mov_b32 s4, 0x4038aa3b
	s_mov_b32 s5, s4
	s_lshl_b32 s40, s26, 6
	s_waitcnt lgkmcnt(0)
	s_lshl_b32 s28, s24, 15
	s_add_u32 s28, s28, 0x1000
	s_add_u32 s10, s10, s28
	s_addc_u32 s11, s11, 0
	s_lshl_b32 s34, s24, 17
	s_lshl_b32 s35, s25, 9
	s_add_u32 s34, s34, s35
	s_add_u32 s34, s14, s34
	s_addc_u32 s35, s15, 0
	s_lshl_b32 s28, s27, 13
	s_add_u32 s28, s8, s28
	s_addc_u32 s29, s9, 0
	s_lshl_b32 s30, s27, 7
	s_add_u32 s30, s12, s30
	s_addc_u32 s31, s13, 0
	global_load_dwordx4 v[2:5], v156, s[10:11] offset:-4096
	global_load_dwordx4 v[6:9], v156, s[10:11] offset:0
	s_add_u32 s10, s10, 0x2000
	s_addc_u32 s11, s11, 0
	global_load_dwordx4 v[10:13], v156, s[10:11] offset:-4096
	global_load_dwordx4 v[14:17], v156, s[10:11] offset:0
	s_add_u32 s10, s10, 0x2000
	s_addc_u32 s11, s11, 0
	global_load_dwordx4 v[18:21], v156, s[10:11] offset:-4096
	global_load_dwordx4 v[22:25], v156, s[10:11] offset:0
	s_add_u32 s10, s10, 0x2000
	s_addc_u32 s11, s11, 0
	global_load_dwordx4 v[26:29], v156, s[10:11] offset:-4096
	global_load_dwordx4 v[30:33], v156, s[10:11] offset:0
	global_load_dwordx4 v[130:133], v160, s[34:35] offset:0
	global_load_dwordx4 v[134:137], v160, s[34:35] offset:128
	global_load_dwordx4 v[138:141], v160, s[34:35] offset:256
	global_load_dwordx4 v[142:145], v160, s[34:35] offset:384
	global_load_dwordx4 v[34:37], v158, s[28:29] offset:0
	global_load_dwordx4 v[38:41], v158, s[28:29] offset:16
	global_load_dwordx4 v[42:45], v158, s[28:29] offset:64
	global_load_dwordx4 v[46:49], v158, s[28:29] offset:80
	global_load_dwordx4 v[50:53], v158, s[28:29] offset:128
	global_load_dwordx4 v[54:57], v158, s[28:29] offset:144
	global_load_dwordx4 v[58:61], v158, s[28:29] offset:192
	global_load_dwordx4 v[62:65], v158, s[28:29] offset:208
	global_load_dwordx4 v[66:69], v159, s[30:31] offset:0
	global_load_dwordx4 v[70:73], v159, s[30:31] offset:32
	global_load_dwordx4 v[74:77], v159, s[30:31] offset:64
	global_load_dwordx4 v[78:81], v159, s[30:31] offset:96
	v_bfe_u32 v163, v0, 1, 3
	v_mul_u32_u24_e32 v163, 0x210, v163
	v_lshrrev_b32_e32 v164, 4, v0
	v_lshl_add_u32 v163, v164, 4, v163
	v_and_b32_e32 v164, 1, v0
	v_lshl_add_u32 v163, v164, 3, v163
	v_lshrrev_b32_e32 v164, 3, v0
	v_mul_u32_u24_e32 v164, 0x110, v164
	v_lshl_add_u32 v164, v161, 3, v164
	v_add_u32_e32 v164, 0x4200, v164
	v_mul_u32_u24_e32 v165, 0x210, v155
	v_lshl_add_u32 v165, v1, 4, v165
	v_mul_u32_u24_e32 v166, 0x110, v1
	v_lshl_add_u32 v166, v155, 4, v166
	v_add_u32_e32 v166, s40, v166
	v_add_u32_e32 v166, 0x4200, v166
	v_mul_u32_u24_e32 v167, 0x880, v155
	v_lshl_add_u32 v167, v1, 1, v167
	v_add_u32_e32 v167, s40, v167
	v_add_u32_e32 v167, 0x4200, v167
	s_lshl_b32 s32, s24, 18
	s_lshl_b32 s33, s27, 11
	s_add_u32 s32, s32, s33
	s_add_u32 s32, s16, s32
	s_addc_u32 s33, s17, 0
	s_lshl_b32 s36, s24, 16
	s_lshl_b32 s37, s25, 13
	s_add_u32 s36, s36, s37
	s_lshl_b32 s37, s26, 11
	s_add_u32 s36, s36, s37
	s_add_u32 s36, s20, s36
	s_addc_u32 s37, s21, 0
	s_lshl_b32 s38, s25, 18
	s_lshl_b32 s39, s26, 16
	s_add_u32 s38, s38, s39
	s_lshl_b32 s39, s24, 11
	s_add_u32 s38, s38, s39
	s_add_u32 s38, s22, s38
	s_addc_u32 s39, s23, 0
	s_waitcnt vmcnt(23)
	v_cvt_pk_f16_f32 v2, v2, v3
	v_cvt_pk_f16_f32 v3, v4, v5
	ds_write_b64 v163, v[2:3] offset:0
	s_waitcnt vmcnt(22)
	v_cvt_pk_f16_f32 v6, v6, v7
	v_cvt_pk_f16_f32 v7, v8, v9
	ds_write_b64 v163, v[6:7] offset:256
	s_waitcnt vmcnt(21)
	v_cvt_pk_f16_f32 v10, v10, v11
	v_cvt_pk_f16_f32 v11, v12, v13
	ds_write_b64 v163, v[10:11] offset:4224
	s_waitcnt vmcnt(20)
	v_cvt_pk_f16_f32 v14, v14, v15
	v_cvt_pk_f16_f32 v15, v16, v17
	ds_write_b64 v163, v[14:15] offset:4480
	s_waitcnt vmcnt(19)
	v_cvt_pk_f16_f32 v18, v18, v19
	v_cvt_pk_f16_f32 v19, v20, v21
	ds_write_b64 v163, v[18:19] offset:8448
	s_waitcnt vmcnt(18)
	v_cvt_pk_f16_f32 v22, v22, v23
	v_cvt_pk_f16_f32 v23, v24, v25
	ds_write_b64 v163, v[22:23] offset:8704
	s_waitcnt vmcnt(17)
	v_cvt_pk_f16_f32 v26, v26, v27
	v_cvt_pk_f16_f32 v27, v28, v29
	ds_write_b64 v163, v[26:27] offset:12672
	s_waitcnt vmcnt(16)
	v_cvt_pk_f16_f32 v30, v30, v31
	v_cvt_pk_f16_f32 v31, v32, v33
	ds_write_b64 v163, v[30:31] offset:12928
	s_waitcnt vmcnt(15)
	v_cvt_pk_f16_f32 v130, v130, v131
	v_cvt_pk_f16_f32 v131, v132, v133
	ds_write_b64 v164, v[130:131] offset:0
	s_waitcnt vmcnt(14)
	v_cvt_pk_f16_f32 v134, v134, v135
	v_cvt_pk_f16_f32 v135, v136, v137
	ds_write_b64 v164, v[134:135] offset:64
	s_waitcnt vmcnt(13)
	v_cvt_pk_f16_f32 v138, v138, v139
	v_cvt_pk_f16_f32 v139, v140, v141
	ds_write_b64 v164, v[138:139] offset:128
	s_waitcnt vmcnt(12)
	v_cvt_pk_f16_f32 v142, v142, v143
	v_cvt_pk_f16_f32 v143, v144, v145
	ds_write_b64 v164, v[142:143] offset:192
	s_waitcnt lgkmcnt(0)
	s_barrier
	ds_read_b128 v[130:133], v166
	ds_read_b128 v[134:137], v166 offset:32
	ds_read_u16 v138, v167 offset:0
	ds_read_u16 v139, v167 offset:272
	ds_read_u16 v140, v167 offset:544
	ds_read_u16 v141, v167 offset:816
	ds_read_u16 v142, v167 offset:1088
	ds_read_u16 v143, v167 offset:1360
	ds_read_u16 v144, v167 offset:1632
	ds_read_u16 v145, v167 offset:1904
	s_waitcnt vmcnt(4)
	v_cvt_pk_f16_f32 v82, v34, v35
	v_cvt_pk_f16_f32 v83, v36, v37
	v_cvt_pk_f16_f32 v84, v38, v39
	v_cvt_pk_f16_f32 v85, v40, v41
	v_cvt_pk_f16_f32 v86, v42, v43
	v_cvt_pk_f16_f32 v87, v44, v45
	v_cvt_pk_f16_f32 v88, v46, v47
	v_cvt_pk_f16_f32 v89, v48, v49
	v_cvt_pk_f16_f32 v90, v50, v51
	v_cvt_pk_f16_f32 v91, v52, v53
	v_cvt_pk_f16_f32 v92, v54, v55
	v_cvt_pk_f16_f32 v93, v56, v57
	v_cvt_pk_f16_f32 v94, v58, v59
	v_cvt_pk_f16_f32 v95, v60, v61
	v_cvt_pk_f16_f32 v96, v62, v63
	v_cvt_pk_f16_f32 v97, v64, v65
	s_waitcnt vmcnt(0)
	v_pk_mul_f32 v[66:67], v[66:67], s[4:5] op_sel_hi:[1,0]
	v_pk_mul_f32 v[68:69], v[68:69], s[4:5] op_sel_hi:[1,0]
	v_pk_mul_f32 v[70:71], v[70:71], s[4:5] op_sel_hi:[1,0]
	v_pk_mul_f32 v[72:73], v[72:73], s[4:5] op_sel_hi:[1,0]
	v_pk_mul_f32 v[74:75], v[74:75], s[4:5] op_sel_hi:[1,0]
	v_pk_mul_f32 v[76:77], v[76:77], s[4:5] op_sel_hi:[1,0]
	v_pk_mul_f32 v[78:79], v[78:79], s[4:5] op_sel_hi:[1,0]
	v_pk_mul_f32 v[80:81], v[80:81], s[4:5] op_sel_hi:[1,0]
	s_waitcnt lgkmcnt(8)
	global_store_dwordx4 v157, v[130:133], s[36:37] sc1
	global_store_dwordx4 v157, v[134:137], s[36:37] offset:1024 sc1
	s_waitcnt lgkmcnt(0)
	v_lshl_or_b32 v138, v139, 16, v138
	v_lshl_or_b32 v139, v141, 16, v140
	v_lshl_or_b32 v140, v143, 16, v142
	v_lshl_or_b32 v141, v145, 16, v144
	global_store_dwordx4 v157, v[138:141], s[38:39] sc1
	ds_read_u16 v142, v167 offset:4352
	ds_read_u16 v143, v167 offset:4624
	ds_read_u16 v144, v167 offset:4896
	ds_read_u16 v145, v167 offset:5168
	ds_read_u16 v146, v167 offset:5440
	ds_read_u16 v147, v167 offset:5712
	ds_read_u16 v148, v167 offset:5984
	ds_read_u16 v149, v167 offset:6256
	ds_read_b128 v[2:5], v165 offset:0
	ds_read_b128 v[6:9], v165 offset:1056
	ds_read_b128 v[10:13], v165 offset:2112
	ds_read_b128 v[14:17], v165 offset:3168
	s_waitcnt lgkmcnt(4)
	v_lshl_or_b32 v142, v143, 16, v142
	v_lshl_or_b32 v143, v145, 16, v144
	v_lshl_or_b32 v144, v147, 16, v146
	v_lshl_or_b32 v145, v149, 16, v148
	global_store_dwordx4 v157, v[142:145], s[38:39] offset:1024 sc1
	ds_read_b128 v[18:21], v165 offset:4224
	ds_read_b128 v[22:25], v165 offset:5280
	ds_read_b128 v[26:29], v165 offset:6336
	ds_read_b128 v[30:33], v165 offset:7392
	ds_read_b128 v[34:37], v165 offset:8448
	ds_read_b128 v[38:41], v165 offset:9504
	ds_read_b128 v[42:45], v165 offset:10560
	ds_read_b128 v[46:49], v165 offset:11616
	s_waitcnt lgkmcnt(8)
	v_mfma_f32_32x32x16_f16 v[98:113], v[82:85], v[2:5], 0
	v_mfma_f32_32x32x16_f16 v[98:113], v[86:89], v[6:9], v[98:113]
	v_mfma_f32_32x32x16_f16 v[98:113], v[90:93], v[10:13], v[98:113]
	v_mfma_f32_32x32x16_f16 v[98:113], v[94:97], v[14:17], v[98:113]
	ds_read_b128 v[50:53], v165 offset:12672
	ds_read_b128 v[54:57], v165 offset:13728
	ds_read_b128 v[58:61], v165 offset:14784
	ds_read_b128 v[62:65], v165 offset:15840
	s_waitcnt lgkmcnt(8)
	v_mfma_f32_32x32x16_f16 v[114:129], v[82:85], v[18:21], 0
	v_mfma_f32_32x32x16_f16 v[114:129], v[86:89], v[22:25], v[114:129]
	v_mfma_f32_32x32x16_f16 v[114:129], v[90:93], v[26:29], v[114:129]
	v_mfma_f32_32x32x16_f16 v[114:129], v[94:97], v[30:33], v[114:129]
	s_nop 7
	v_pk_fma_f32 v[130:131], v[98:99], s[4:5], v[66:67] op_sel_hi:[1,0,1]
	v_pk_fma_f32 v[132:133], v[100:101], s[4:5], v[68:69] op_sel_hi:[1,0,1]
	v_pk_fma_f32 v[134:135], v[102:103], s[4:5], v[70:71] op_sel_hi:[1,0,1]
	v_pk_fma_f32 v[136:137], v[104:105], s[4:5], v[72:73] op_sel_hi:[1,0,1]
	v_pk_fma_f32 v[138:139], v[106:107], s[4:5], v[74:75] op_sel_hi:[1,0,1]
	v_pk_fma_f32 v[140:141], v[108:109], s[4:5], v[76:77] op_sel_hi:[1,0,1]
	v_pk_fma_f32 v[142:143], v[110:111], s[4:5], v[78:79] op_sel_hi:[1,0,1]
	v_pk_fma_f32 v[144:145], v[112:113], s[4:5], v[80:81] op_sel_hi:[1,0,1]
	v_exp_f32_e32 v130, v130
	v_exp_f32_e32 v131, v131
	v_exp_f32_e32 v132, v132
	v_exp_f32_e32 v133, v133
	v_exp_f32_e32 v134, v134
	v_exp_f32_e32 v135, v135
	v_exp_f32_e32 v136, v136
	v_exp_f32_e32 v137, v137
	v_exp_f32_e32 v138, v138
	v_exp_f32_e32 v139, v139
	v_exp_f32_e32 v140, v140
	v_exp_f32_e32 v141, v141
	v_exp_f32_e32 v142, v142
	v_exp_f32_e32 v143, v143
	v_exp_f32_e32 v144, v144
	v_exp_f32_e32 v145, v145
	v_pk_add_f32 v[130:131], v[130:131], 1.0 op_sel_hi:[1,0]
	v_pk_add_f32 v[132:133], v[132:133], 1.0 op_sel_hi:[1,0]
	v_pk_add_f32 v[134:135], v[134:135], 1.0 op_sel_hi:[1,0]
	v_pk_add_f32 v[136:137], v[136:137], 1.0 op_sel_hi:[1,0]
	v_pk_add_f32 v[138:139], v[138:139], 1.0 op_sel_hi:[1,0]
	v_pk_add_f32 v[140:141], v[140:141], 1.0 op_sel_hi:[1,0]
	v_pk_add_f32 v[142:143], v[142:143], 1.0 op_sel_hi:[1,0]
	v_pk_add_f32 v[144:145], v[144:145], 1.0 op_sel_hi:[1,0]
	v_rcp_f32_e32 v130, v130
	v_rcp_f32_e32 v131, v131
	v_rcp_f32_e32 v132, v132
	v_rcp_f32_e32 v133, v133
	v_rcp_f32_e32 v134, v134
	v_rcp_f32_e32 v135, v135
	v_rcp_f32_e32 v136, v136
	v_rcp_f32_e32 v137, v137
	v_rcp_f32_e32 v138, v138
	v_rcp_f32_e32 v139, v139
	v_rcp_f32_e32 v140, v140
	v_rcp_f32_e32 v141, v141
	v_rcp_f32_e32 v142, v142
	v_rcp_f32_e32 v143, v143
	v_rcp_f32_e32 v144, v144
	v_rcp_f32_e32 v145, v145
	v_pk_fma_f32 v[130:131], v[130:131], 2.0, 1.0 op_sel_hi:[1,0,0] neg_lo:[1,0,0] neg_hi:[1,0,0]
	v_pk_fma_f32 v[132:133], v[132:133], 2.0, 1.0 op_sel_hi:[1,0,0] neg_lo:[1,0,0] neg_hi:[1,0,0]
	v_pk_fma_f32 v[134:135], v[134:135], 2.0, 1.0 op_sel_hi:[1,0,0] neg_lo:[1,0,0] neg_hi:[1,0,0]
	v_pk_fma_f32 v[136:137], v[136:137], 2.0, 1.0 op_sel_hi:[1,0,0] neg_lo:[1,0,0] neg_hi:[1,0,0]
	v_pk_fma_f32 v[138:139], v[138:139], 2.0, 1.0 op_sel_hi:[1,0,0] neg_lo:[1,0,0] neg_hi:[1,0,0]
	v_pk_fma_f32 v[140:141], v[140:141], 2.0, 1.0 op_sel_hi:[1,0,0] neg_lo:[1,0,0] neg_hi:[1,0,0]
	v_pk_fma_f32 v[142:143], v[142:143], 2.0, 1.0 op_sel_hi:[1,0,0] neg_lo:[1,0,0] neg_hi:[1,0,0]
	v_pk_fma_f32 v[144:145], v[144:145], 2.0, 1.0 op_sel_hi:[1,0,0] neg_lo:[1,0,0] neg_hi:[1,0,0]
	v_cvt_pk_f16_f32 v146, v130, v131
	v_cvt_pk_f16_f32 v147, v132, v133
	v_cvt_pk_f16_f32 v148, v134, v135
	v_cvt_pk_f16_f32 v149, v136, v137
	v_cvt_pk_f16_f32 v150, v138, v139
	v_cvt_pk_f16_f32 v151, v140, v141
	v_cvt_pk_f16_f32 v152, v142, v143
	v_cvt_pk_f16_f32 v153, v144, v145
	s_nop 1
	v_permlane32_swap_b32_e32 v146, v148
	v_permlane32_swap_b32_e32 v147, v149
	v_permlane32_swap_b32_e32 v150, v152
	v_permlane32_swap_b32_e32 v151, v153
	global_store_dwordx4 v157, v[146:149], s[32:33] sc1
	global_store_dwordx4 v157, v[150:153], s[32:33] offset:1024 sc1
	s_add_u32 s32, s32, 0x10000
	s_addc_u32 s33, s33, 0
	s_waitcnt lgkmcnt(4)
	v_mfma_f32_32x32x16_f16 v[98:113], v[82:85], v[34:37], 0
	v_mfma_f32_32x32x16_f16 v[98:113], v[86:89], v[38:41], v[98:113]
	v_mfma_f32_32x32x16_f16 v[98:113], v[90:93], v[42:45], v[98:113]
	v_mfma_f32_32x32x16_f16 v[98:113], v[94:97], v[46:49], v[98:113]
	v_pk_fma_f32 v[130:131], v[114:115], s[4:5], v[66:67] op_sel_hi:[1,0,1]
	v_pk_fma_f32 v[132:133], v[116:117], s[4:5], v[68:69] op_sel_hi:[1,0,1]
	v_pk_fma_f32 v[134:135], v[118:119], s[4:5], v[70:71] op_sel_hi:[1,0,1]
	v_pk_fma_f32 v[136:137], v[120:121], s[4:5], v[72:73] op_sel_hi:[1,0,1]
	v_pk_fma_f32 v[138:139], v[122:123], s[4:5], v[74:75] op_sel_hi:[1,0,1]
	v_pk_fma_f32 v[140:141], v[124:125], s[4:5], v[76:77] op_sel_hi:[1,0,1]
	v_pk_fma_f32 v[142:143], v[126:127], s[4:5], v[78:79] op_sel_hi:[1,0,1]
	v_pk_fma_f32 v[144:145], v[128:129], s[4:5], v[80:81] op_sel_hi:[1,0,1]
	v_exp_f32_e32 v130, v130
	v_exp_f32_e32 v131, v131
	v_exp_f32_e32 v132, v132
	v_exp_f32_e32 v133, v133
	v_exp_f32_e32 v134, v134
	v_exp_f32_e32 v135, v135
	v_exp_f32_e32 v136, v136
	v_exp_f32_e32 v137, v137
	v_exp_f32_e32 v138, v138
	v_exp_f32_e32 v139, v139
	v_exp_f32_e32 v140, v140
	v_exp_f32_e32 v141, v141
	v_exp_f32_e32 v142, v142
	v_exp_f32_e32 v143, v143
	v_exp_f32_e32 v144, v144
	v_exp_f32_e32 v145, v145
	v_pk_add_f32 v[130:131], v[130:131], 1.0 op_sel_hi:[1,0]
	v_pk_add_f32 v[132:133], v[132:133], 1.0 op_sel_hi:[1,0]
	v_pk_add_f32 v[134:135], v[134:135], 1.0 op_sel_hi:[1,0]
	v_pk_add_f32 v[136:137], v[136:137], 1.0 op_sel_hi:[1,0]
	v_pk_add_f32 v[138:139], v[138:139], 1.0 op_sel_hi:[1,0]
	v_pk_add_f32 v[140:141], v[140:141], 1.0 op_sel_hi:[1,0]
	v_pk_add_f32 v[142:143], v[142:143], 1.0 op_sel_hi:[1,0]
	v_pk_add_f32 v[144:145], v[144:145], 1.0 op_sel_hi:[1,0]
	v_rcp_f32_e32 v130, v130
	v_rcp_f32_e32 v131, v131
	v_rcp_f32_e32 v132, v132
	v_rcp_f32_e32 v133, v133
	v_rcp_f32_e32 v134, v134
	v_rcp_f32_e32 v135, v135
	v_rcp_f32_e32 v136, v136
	v_rcp_f32_e32 v137, v137
	v_rcp_f32_e32 v138, v138
	v_rcp_f32_e32 v139, v139
	v_rcp_f32_e32 v140, v140
	v_rcp_f32_e32 v141, v141
	v_rcp_f32_e32 v142, v142
	v_rcp_f32_e32 v143, v143
	v_rcp_f32_e32 v144, v144
	v_rcp_f32_e32 v145, v145
	v_pk_fma_f32 v[130:131], v[130:131], 2.0, 1.0 op_sel_hi:[1,0,0] neg_lo:[1,0,0] neg_hi:[1,0,0]
	v_pk_fma_f32 v[132:133], v[132:133], 2.0, 1.0 op_sel_hi:[1,0,0] neg_lo:[1,0,0] neg_hi:[1,0,0]
	v_pk_fma_f32 v[134:135], v[134:135], 2.0, 1.0 op_sel_hi:[1,0,0] neg_lo:[1,0,0] neg_hi:[1,0,0]
	v_pk_fma_f32 v[136:137], v[136:137], 2.0, 1.0 op_sel_hi:[1,0,0] neg_lo:[1,0,0] neg_hi:[1,0,0]
	v_pk_fma_f32 v[138:139], v[138:139], 2.0, 1.0 op_sel_hi:[1,0,0] neg_lo:[1,0,0] neg_hi:[1,0,0]
	v_pk_fma_f32 v[140:141], v[140:141], 2.0, 1.0 op_sel_hi:[1,0,0] neg_lo:[1,0,0] neg_hi:[1,0,0]
	v_pk_fma_f32 v[142:143], v[142:143], 2.0, 1.0 op_sel_hi:[1,0,0] neg_lo:[1,0,0] neg_hi:[1,0,0]
	v_pk_fma_f32 v[144:145], v[144:145], 2.0, 1.0 op_sel_hi:[1,0,0] neg_lo:[1,0,0] neg_hi:[1,0,0]
	v_cvt_pk_f16_f32 v146, v130, v131
	v_cvt_pk_f16_f32 v147, v132, v133
	v_cvt_pk_f16_f32 v148, v134, v135
	v_cvt_pk_f16_f32 v149, v136, v137
	v_cvt_pk_f16_f32 v150, v138, v139
	v_cvt_pk_f16_f32 v151, v140, v141
	v_cvt_pk_f16_f32 v152, v142, v143
	v_cvt_pk_f16_f32 v153, v144, v145
	s_nop 1
	v_permlane32_swap_b32_e32 v146, v148
	v_permlane32_swap_b32_e32 v147, v149
	v_permlane32_swap_b32_e32 v150, v152
	v_permlane32_swap_b32_e32 v151, v153
	global_store_dwordx4 v157, v[146:149], s[32:33] sc1
	global_store_dwordx4 v157, v[150:153], s[32:33] offset:1024 sc1
	s_add_u32 s32, s32, 0x10000
	s_addc_u32 s33, s33, 0
	s_waitcnt lgkmcnt(0)
	v_mfma_f32_32x32x16_f16 v[114:129], v[82:85], v[50:53], 0
	v_mfma_f32_32x32x16_f16 v[114:129], v[86:89], v[54:57], v[114:129]
	v_mfma_f32_32x32x16_f16 v[114:129], v[90:93], v[58:61], v[114:129]
	v_mfma_f32_32x32x16_f16 v[114:129], v[94:97], v[62:65], v[114:129]
	v_pk_fma_f32 v[130:131], v[98:99], s[4:5], v[66:67] op_sel_hi:[1,0,1]
	v_pk_fma_f32 v[132:133], v[100:101], s[4:5], v[68:69] op_sel_hi:[1,0,1]
	v_pk_fma_f32 v[134:135], v[102:103], s[4:5], v[70:71] op_sel_hi:[1,0,1]
	v_pk_fma_f32 v[136:137], v[104:105], s[4:5], v[72:73] op_sel_hi:[1,0,1]
	v_pk_fma_f32 v[138:139], v[106:107], s[4:5], v[74:75] op_sel_hi:[1,0,1]
	v_pk_fma_f32 v[140:141], v[108:109], s[4:5], v[76:77] op_sel_hi:[1,0,1]
	v_pk_fma_f32 v[142:143], v[110:111], s[4:5], v[78:79] op_sel_hi:[1,0,1]
	v_pk_fma_f32 v[144:145], v[112:113], s[4:5], v[80:81] op_sel_hi:[1,0,1]
	v_exp_f32_e32 v130, v130
	v_exp_f32_e32 v131, v131
	v_exp_f32_e32 v132, v132
	v_exp_f32_e32 v133, v133
	v_exp_f32_e32 v134, v134
	v_exp_f32_e32 v135, v135
	v_exp_f32_e32 v136, v136
	v_exp_f32_e32 v137, v137
	v_exp_f32_e32 v138, v138
	v_exp_f32_e32 v139, v139
	v_exp_f32_e32 v140, v140
	v_exp_f32_e32 v141, v141
	v_exp_f32_e32 v142, v142
	v_exp_f32_e32 v143, v143
	v_exp_f32_e32 v144, v144
	v_exp_f32_e32 v145, v145
	v_pk_add_f32 v[130:131], v[130:131], 1.0 op_sel_hi:[1,0]
	v_pk_add_f32 v[132:133], v[132:133], 1.0 op_sel_hi:[1,0]
	v_pk_add_f32 v[134:135], v[134:135], 1.0 op_sel_hi:[1,0]
	v_pk_add_f32 v[136:137], v[136:137], 1.0 op_sel_hi:[1,0]
	v_pk_add_f32 v[138:139], v[138:139], 1.0 op_sel_hi:[1,0]
	v_pk_add_f32 v[140:141], v[140:141], 1.0 op_sel_hi:[1,0]
	v_pk_add_f32 v[142:143], v[142:143], 1.0 op_sel_hi:[1,0]
	v_pk_add_f32 v[144:145], v[144:145], 1.0 op_sel_hi:[1,0]
	v_rcp_f32_e32 v130, v130
	v_rcp_f32_e32 v131, v131
	v_rcp_f32_e32 v132, v132
	v_rcp_f32_e32 v133, v133
	v_rcp_f32_e32 v134, v134
	v_rcp_f32_e32 v135, v135
	v_rcp_f32_e32 v136, v136
	v_rcp_f32_e32 v137, v137
	v_rcp_f32_e32 v138, v138
	v_rcp_f32_e32 v139, v139
	v_rcp_f32_e32 v140, v140
	v_rcp_f32_e32 v141, v141
	v_rcp_f32_e32 v142, v142
	v_rcp_f32_e32 v143, v143
	v_rcp_f32_e32 v144, v144
	v_rcp_f32_e32 v145, v145
	v_pk_fma_f32 v[130:131], v[130:131], 2.0, 1.0 op_sel_hi:[1,0,0] neg_lo:[1,0,0] neg_hi:[1,0,0]
	v_pk_fma_f32 v[132:133], v[132:133], 2.0, 1.0 op_sel_hi:[1,0,0] neg_lo:[1,0,0] neg_hi:[1,0,0]
	v_pk_fma_f32 v[134:135], v[134:135], 2.0, 1.0 op_sel_hi:[1,0,0] neg_lo:[1,0,0] neg_hi:[1,0,0]
	v_pk_fma_f32 v[136:137], v[136:137], 2.0, 1.0 op_sel_hi:[1,0,0] neg_lo:[1,0,0] neg_hi:[1,0,0]
	v_pk_fma_f32 v[138:139], v[138:139], 2.0, 1.0 op_sel_hi:[1,0,0] neg_lo:[1,0,0] neg_hi:[1,0,0]
	v_pk_fma_f32 v[140:141], v[140:141], 2.0, 1.0 op_sel_hi:[1,0,0] neg_lo:[1,0,0] neg_hi:[1,0,0]
	v_pk_fma_f32 v[142:143], v[142:143], 2.0, 1.0 op_sel_hi:[1,0,0] neg_lo:[1,0,0] neg_hi:[1,0,0]
	v_pk_fma_f32 v[144:145], v[144:145], 2.0, 1.0 op_sel_hi:[1,0,0] neg_lo:[1,0,0] neg_hi:[1,0,0]
	v_cvt_pk_f16_f32 v146, v130, v131
	v_cvt_pk_f16_f32 v147, v132, v133
	v_cvt_pk_f16_f32 v148, v134, v135
	v_cvt_pk_f16_f32 v149, v136, v137
	v_cvt_pk_f16_f32 v150, v138, v139
	v_cvt_pk_f16_f32 v151, v140, v141
	v_cvt_pk_f16_f32 v152, v142, v143
	v_cvt_pk_f16_f32 v153, v144, v145
	s_nop 1
	v_permlane32_swap_b32_e32 v146, v148
	v_permlane32_swap_b32_e32 v147, v149
	v_permlane32_swap_b32_e32 v150, v152
	v_permlane32_swap_b32_e32 v151, v153
	global_store_dwordx4 v157, v[146:149], s[32:33] sc1
	global_store_dwordx4 v157, v[150:153], s[32:33] offset:1024 sc1
	s_add_u32 s32, s32, 0x10000
	s_addc_u32 s33, s33, 0
	s_nop 7
	v_pk_fma_f32 v[130:131], v[114:115], s[4:5], v[66:67] op_sel_hi:[1,0,1]
	v_pk_fma_f32 v[132:133], v[116:117], s[4:5], v[68:69] op_sel_hi:[1,0,1]
	v_pk_fma_f32 v[134:135], v[118:119], s[4:5], v[70:71] op_sel_hi:[1,0,1]
	v_pk_fma_f32 v[136:137], v[120:121], s[4:5], v[72:73] op_sel_hi:[1,0,1]
	v_pk_fma_f32 v[138:139], v[122:123], s[4:5], v[74:75] op_sel_hi:[1,0,1]
	v_pk_fma_f32 v[140:141], v[124:125], s[4:5], v[76:77] op_sel_hi:[1,0,1]
	v_pk_fma_f32 v[142:143], v[126:127], s[4:5], v[78:79] op_sel_hi:[1,0,1]
	v_pk_fma_f32 v[144:145], v[128:129], s[4:5], v[80:81] op_sel_hi:[1,0,1]
	v_exp_f32_e32 v130, v130
	v_exp_f32_e32 v131, v131
	v_exp_f32_e32 v132, v132
	v_exp_f32_e32 v133, v133
	v_exp_f32_e32 v134, v134
	v_exp_f32_e32 v135, v135
	v_exp_f32_e32 v136, v136
	v_exp_f32_e32 v137, v137
	v_exp_f32_e32 v138, v138
	v_exp_f32_e32 v139, v139
	v_exp_f32_e32 v140, v140
	v_exp_f32_e32 v141, v141
	v_exp_f32_e32 v142, v142
	v_exp_f32_e32 v143, v143
	v_exp_f32_e32 v144, v144
	v_exp_f32_e32 v145, v145
	v_pk_add_f32 v[130:131], v[130:131], 1.0 op_sel_hi:[1,0]
	v_pk_add_f32 v[132:133], v[132:133], 1.0 op_sel_hi:[1,0]
	v_pk_add_f32 v[134:135], v[134:135], 1.0 op_sel_hi:[1,0]
	v_pk_add_f32 v[136:137], v[136:137], 1.0 op_sel_hi:[1,0]
	v_pk_add_f32 v[138:139], v[138:139], 1.0 op_sel_hi:[1,0]
	v_pk_add_f32 v[140:141], v[140:141], 1.0 op_sel_hi:[1,0]
	v_pk_add_f32 v[142:143], v[142:143], 1.0 op_sel_hi:[1,0]
	v_pk_add_f32 v[144:145], v[144:145], 1.0 op_sel_hi:[1,0]
	v_rcp_f32_e32 v130, v130
	v_rcp_f32_e32 v131, v131
	v_rcp_f32_e32 v132, v132
	v_rcp_f32_e32 v133, v133
	v_rcp_f32_e32 v134, v134
	v_rcp_f32_e32 v135, v135
	v_rcp_f32_e32 v136, v136
	v_rcp_f32_e32 v137, v137
	v_rcp_f32_e32 v138, v138
	v_rcp_f32_e32 v139, v139
	v_rcp_f32_e32 v140, v140
	v_rcp_f32_e32 v141, v141
	v_rcp_f32_e32 v142, v142
	v_rcp_f32_e32 v143, v143
	v_rcp_f32_e32 v144, v144
	v_rcp_f32_e32 v145, v145
	v_pk_fma_f32 v[130:131], v[130:131], 2.0, 1.0 op_sel_hi:[1,0,0] neg_lo:[1,0,0] neg_hi:[1,0,0]
	v_pk_fma_f32 v[132:133], v[132:133], 2.0, 1.0 op_sel_hi:[1,0,0] neg_lo:[1,0,0] neg_hi:[1,0,0]
	v_pk_fma_f32 v[134:135], v[134:135], 2.0, 1.0 op_sel_hi:[1,0,0] neg_lo:[1,0,0] neg_hi:[1,0,0]
	v_pk_fma_f32 v[136:137], v[136:137], 2.0, 1.0 op_sel_hi:[1,0,0] neg_lo:[1,0,0] neg_hi:[1,0,0]
	v_pk_fma_f32 v[138:139], v[138:139], 2.0, 1.0 op_sel_hi:[1,0,0] neg_lo:[1,0,0] neg_hi:[1,0,0]
	v_pk_fma_f32 v[140:141], v[140:141], 2.0, 1.0 op_sel_hi:[1,0,0] neg_lo:[1,0,0] neg_hi:[1,0,0]
	v_pk_fma_f32 v[142:143], v[142:143], 2.0, 1.0 op_sel_hi:[1,0,0] neg_lo:[1,0,0] neg_hi:[1,0,0]
	v_pk_fma_f32 v[144:145], v[144:145], 2.0, 1.0 op_sel_hi:[1,0,0] neg_lo:[1,0,0] neg_hi:[1,0,0]
	v_cvt_pk_f16_f32 v146, v130, v131
	v_cvt_pk_f16_f32 v147, v132, v133
	v_cvt_pk_f16_f32 v148, v134, v135
	v_cvt_pk_f16_f32 v149, v136, v137
	v_cvt_pk_f16_f32 v150, v138, v139
	v_cvt_pk_f16_f32 v151, v140, v141
	v_cvt_pk_f16_f32 v152, v142, v143
	v_cvt_pk_f16_f32 v153, v144, v145
	s_nop 1
	v_permlane32_swap_b32_e32 v146, v148
	v_permlane32_swap_b32_e32 v147, v149
	v_permlane32_swap_b32_e32 v150, v152
	v_permlane32_swap_b32_e32 v151, v153
	global_store_dwordx4 v157, v[146:149], s[32:33] sc1
	global_store_dwordx4 v157, v[150:153], s[32:33] offset:1024 sc1
	s_endpgm
.Lp_w1t:
	s_load_dwordx2 s[16:17], s[0:1], 0x38
	s_load_dwordx2 s[18:19], s[0:1], 0x40
	s_load_dwordx4 s[20:23], s[0:1], 0x48
	v_lshl_or_b32 v2, s2, 8, v0
	v_add_u32_e32 v2, 0xfffec000, v2
	v_mov_b32_e32 v3, 0
	v_mov_b32_e32 v26, v0
	v_lshrrev_b32_e32 v4, 3, v2
	v_lshrrev_b32_e32 v5, 3, v0
	v_lshlrev_b32_e32 v0, 1, v0
	v_and_b32_e32 v4, 0x1fffffe0, v4
	v_and_b32_e32 v6, 0x80, v0
	v_mov_b32_e32 v7, 0
	v_and_or_b32 v4, v5, 20, v4
	s_waitcnt lgkmcnt(0)
	v_lshl_add_u64 v[8:9], s[8:9], 0, v[6:7]
	v_lshlrev_b32_e32 v6, 2, v1
	v_lshl_add_u64 v[0:1], v[8:9], 0, v[6:7]
	v_or_b32_e32 v6, 1, v4
	v_lshlrev_b64 v[10:11], 8, v[6:7]
	v_or_b32_e32 v6, 2, v4
	v_lshlrev_b64 v[12:13], 8, v[6:7]
	v_or_b32_e32 v6, 3, v4
	v_lshlrev_b64 v[14:15], 8, v[6:7]
	v_or_b32_e32 v6, 8, v4
	v_lshlrev_b64 v[16:17], 8, v[6:7]
	v_or_b32_e32 v6, 9, v4
	v_mov_b32_e32 v5, v7
	v_lshlrev_b64 v[18:19], 8, v[6:7]
	v_or_b32_e32 v6, 10, v4
	v_lshlrev_b64 v[8:9], 8, v[4:5]
	v_lshlrev_b64 v[20:21], 8, v[6:7]
	v_or_b32_e32 v6, 11, v4
	v_lshl_add_u64 v[8:9], v[0:1], 0, v[8:9]
	v_lshlrev_b64 v[4:5], 8, v[6:7]
	v_lshl_add_u64 v[10:11], v[0:1], 0, v[10:11]
	v_lshl_add_u64 v[12:13], v[0:1], 0, v[12:13]
	v_lshl_add_u64 v[14:15], v[0:1], 0, v[14:15]
	v_lshl_add_u64 v[16:17], v[0:1], 0, v[16:17]
	v_lshl_add_u64 v[18:19], v[0:1], 0, v[18:19]
	v_lshl_add_u64 v[20:21], v[0:1], 0, v[20:21]
	v_lshl_add_u64 v[0:1], v[0:1], 0, v[4:5]
	global_load_dword v4, v[8:9], off
	global_load_dword v5, v[10:11], off
	global_load_dword v6, v[12:13], off
	global_load_dword v7, v[14:15], off
	global_load_dword v22, v[16:17], off
	global_load_dword v23, v[18:19], off
	global_load_dword v24, v[20:21], off
	global_load_dword v25, v[0:1], off
	v_lshl_add_u64 v[0:1], v[2:3], 4, s[16:17]
	v_lshlrev_b64 v[28:29], 7, v[2:3]
	v_lshl_add_u64 v[28:29], s[18:19], 0, v[28:29]
	global_load_dword v30, v[28:29], off
	s_getpc_b64 s[24:25]
	s_and_b32 s24, s24, 0xfffff000
	v_lshlrev_b32_e32 v32, 7, v26
	v_mov_b32_e32 v33, 0
	v_lshl_add_u64 v[34:35], s[24:25], 0, v[32:33]
	global_load_dword v31, v[34:35], off sc0 sc1
	s_waitcnt vmcnt(2)
	v_cvt_pk_f16_f32 v4, v4, v5
	v_cvt_pk_f16_f32 v5, v6, v7
	v_cvt_pk_f16_f32 v6, v22, v23
	v_cvt_pk_f16_f32 v7, v24, v25
	global_store_dwordx4 v[0:1], v[4:7], off sc1
	s_movk_i32 s4, 0x70
	v_cmp_gt_u32_e32 vcc, s4, v26
	s_and_saveexec_b64 s[4:5], vcc
	s_cbranch_execz .Lp_t1
	v_add_co_u32_e32 v34, vcc, 0x8000, v34
	s_nop 1
	v_addc_co_u32_e32 v35, vcc, 0, v35, vcc
	global_load_dword v8, v[34:35], off sc0 sc1
.Lp_t1:
	s_or_b64 exec, exec, s[4:5]
	s_movk_i32 s4, 0xdf
	v_cmp_lt_u32_e32 vcc, s4, v26
	s_and_saveexec_b64 s[4:5], vcc
	s_cbranch_execz .Lp_t2
	s_and_b32 s0, s0, 0xfffff000
	v_lshl_add_u64 v[36:37], s[0:1], 0, v[32:33]
	v_add_co_u32_e32 v36, vcc, 0xffff9000, v36
	s_nop 1
	v_addc_co_u32_e32 v37, vcc, -1, v37, vcc
	global_load_dword v9, v[36:37], off sc0 sc1
.Lp_t2:
	s_or_b64 exec, exec, s[4:5]
	v_cmp_gt_u32_e32 vcc, 32, v2
	s_and_saveexec_b64 s[4:5], vcc
	s_cbranch_execz .Lp_t3
	v_lshlrev_b64 v[10:11], 7, v[2:3]
	v_lshl_add_u64 v[10:11], s[20:21], 0, v[10:11]
	global_load_dword v12, v[10:11], off
.Lp_t3:
	s_or_b64 exec, exec, s[4:5]
	v_add_u32_e32 v13, 0xffffffe0, v2
	v_cmp_gt_u32_e32 vcc, 32, v13
	s_and_saveexec_b64 s[4:5], vcc
	s_cbranch_execz .Lp_t4
	v_lshlrev_b64 v[10:11], 7, v[2:3]
	v_lshl_add_u64 v[10:11], s[22:23], 0, v[10:11]
	global_load_dword v14, v[10:11], off offset:-4096
.Lp_t4:
	s_endpgm
	.section	.rodata,"a",@progbits
	.p2align	6, 0x0

.LBB3_4:
	s_load_dwordx2 s[6:7], s[0:1], 0x0
	s_load_dwordx2 s[2:3], s[0:1], 0x38
	s_lshr_b32 s0, s8, 6
	s_lshl_b32 s1, s4, 8
	s_lshl_b32 s8, s5, 7
	s_add_i32 s8, s8, s1
	s_ashr_i32 s9, s8, 31
	s_lshl_b64 s[8:9], s[8:9], 10
	s_waitcnt lgkmcnt(0)
	s_add_u32 s6, s6, s8
	s_addc_u32 s7, s7, s9
	v_mov_b32_e32 v135, 0
	v_lshl_add_u64 v[2:3], s[6:7], 0, v[134:135]
	s_mov_b32 s1, 0x10000
	v_add_co_u32_e32 v36, vcc, s1, v2
	s_mov_b32 s1, 0x11000
	s_nop 0
	v_addc_co_u32_e32 v37, vcc, 0, v3, vcc
	v_add_co_u32_e32 v68, vcc, s1, v2
	global_load_dwordx4 v[4:7], v134, s[6:7]
	global_load_dwordx4 v[8:11], v134, s[6:7] offset:1024
	global_load_dwordx4 v[12:15], v134, s[6:7] offset:2048
	v_addc_co_u32_e32 v69, vcc, 0, v3, vcc
	global_load_dwordx4 v[16:19], v134, s[6:7] offset:3072
	global_load_dwordx4 v[20:23], v[68:69], off offset:-4096
	global_load_dwordx4 v[24:27], v[36:37], off offset:1024
	global_load_dwordx4 v[28:31], v[36:37], off offset:2048
	global_load_dwordx4 v[32:35], v[36:37], off offset:3072
	s_movk_i32 s7, 0x2000
	v_add_co_u32_e32 v100, vcc, s7, v2
	s_movk_i32 s6, 0x1000
	s_nop 0
	v_addc_co_u32_e32 v101, vcc, 0, v3, vcc
	v_add_co_u32_e32 v70, vcc, s6, v2
	global_load_dwordx4 v[36:39], v[100:101], off offset:-4096
	s_nop 0
	v_addc_co_u32_e32 v71, vcc, 0, v3, vcc
	global_load_dwordx4 v[40:43], v[70:71], off offset:1024
	global_load_dwordx4 v[44:47], v[70:71], off offset:2048
	global_load_dwordx4 v[48:51], v[70:71], off offset:3072
	global_load_dwordx4 v[52:55], v[68:69], off
	global_load_dwordx4 v[56:59], v[68:69], off offset:1024
	global_load_dwordx4 v[60:63], v[68:69], off offset:2048
	global_load_dwordx4 v[64:67], v[68:69], off offset:3072
	s_mov_b32 s1, 0x12000
	v_add_co_u32_e32 v102, vcc, s1, v2
	s_mov_b32 s8, 0x13000
	s_nop 0
	v_addc_co_u32_e32 v103, vcc, 0, v3, vcc
	v_add_co_u32_e32 v104, vcc, s8, v2
	s_movk_i32 s9, 0x4000
	s_nop 0
	v_addc_co_u32_e32 v105, vcc, 0, v3, vcc
	v_add_co_u32_e32 v106, vcc, s9, v2
	global_load_dwordx4 v[68:71], v[100:101], off
	global_load_dwordx4 v[72:75], v[100:101], off offset:1024
	global_load_dwordx4 v[76:79], v[100:101], off offset:2048
	global_load_dwordx4 v[80:83], v[100:101], off offset:3072
	global_load_dwordx4 v[84:87], v[104:105], off offset:-4096
	global_load_dwordx4 v[88:91], v[102:103], off offset:1024
	global_load_dwordx4 v[92:95], v[102:103], off offset:2048
	global_load_dwordx4 v[96:99], v[102:103], off offset:3072
	v_lshl_or_b32 v1, s5, 13, v134
	s_movk_i32 s5, 0x3000
	v_addc_co_u32_e32 v107, vcc, 0, v3, vcc
	v_add_co_u32_e32 v108, vcc, s5, v2
	s_mov_b32 s8, 0x14000
	s_nop 0
	v_addc_co_u32_e32 v109, vcc, 0, v3, vcc
	s_ashr_i32 s5, s4, 31
	s_lshl_b32 s10, s0, 13
	s_lshl_b64 s[0:1], s[4:5], 14
	v_add_co_u32_e32 v100, vcc, s8, v2
	s_mov_b32 s9, 0x15000
	s_add_u32 s0, s2, s0
	v_addc_co_u32_e32 v101, vcc, 0, v3, vcc
	s_addc_u32 s1, s3, s1
	s_and_b32 s2, s10, 0x6000
	v_add_co_u32_e32 v102, vcc, s9, v2
	s_movk_i32 s3, 0x5000
	s_nop 0
	v_addc_co_u32_e32 v103, vcc, 0, v3, vcc
	s_waitcnt vmcnt(23)
	ds_write_b128 v1, v[4:7]
	s_waitcnt vmcnt(22)
	ds_write_b128 v1, v[8:11] offset:1024
	s_waitcnt vmcnt(21)
	ds_write_b128 v1, v[12:15] offset:2048
	s_waitcnt vmcnt(20)
	ds_write_b128 v1, v[16:19] offset:3072
	s_waitcnt vmcnt(19)
	ds_write_b128 v1, v[20:23] offset:4096
	s_waitcnt vmcnt(18)
	ds_write_b128 v1, v[24:27] offset:5120
	s_waitcnt vmcnt(17)
	ds_write_b128 v1, v[28:31] offset:6144
	s_waitcnt vmcnt(16)
	ds_write_b128 v1, v[32:35] offset:7168
	s_waitcnt lgkmcnt(0)
	s_barrier
	global_load_dwordx4 v[4:7], v[106:107], off offset:-4096
	global_load_dwordx4 v[8:11], v[108:109], off offset:1024
	global_load_dwordx4 v[12:15], v[108:109], off offset:2048
	global_load_dwordx4 v[16:19], v[108:109], off offset:3072
	global_load_dwordx4 v[20:23], v[104:105], off
	global_load_dwordx4 v[24:27], v[104:105], off offset:1024
	global_load_dwordx4 v[28:31], v[104:105], off offset:2048
	global_load_dwordx4 v[32:35], v[104:105], off offset:3072
	v_or_b32_e32 v1, s2, v134
	s_waitcnt vmcnt(23)
	ds_write_b128 v1, v[36:39] offset:16384
	s_waitcnt vmcnt(22)
	ds_write_b128 v1, v[40:43] offset:17408
	s_waitcnt vmcnt(21)
	ds_write_b128 v1, v[44:47] offset:18432
	s_waitcnt vmcnt(20)
	ds_write_b128 v1, v[48:51] offset:19456
	s_waitcnt vmcnt(19)
	ds_write_b128 v1, v[52:55] offset:20480
	s_waitcnt vmcnt(18)
	ds_write_b128 v1, v[56:59] offset:21504
	s_waitcnt vmcnt(17)
	ds_write_b128 v1, v[60:63] offset:22528
	s_waitcnt vmcnt(16)
	ds_write_b128 v1, v[64:67] offset:23552
	s_waitcnt lgkmcnt(0)
	s_barrier
	global_load_dwordx4 v[36:39], v[106:107], off
	global_load_dwordx4 v[40:43], v[106:107], off offset:1024
	global_load_dwordx4 v[44:47], v[106:107], off offset:2048
	global_load_dwordx4 v[48:51], v[106:107], off offset:3072
	global_load_dwordx4 v[52:55], v[102:103], off offset:-4096
	global_load_dwordx4 v[56:59], v[100:101], off offset:1024
	global_load_dwordx4 v[60:63], v[100:101], off offset:2048
	global_load_dwordx4 v[64:67], v[100:101], off offset:3072
	s_movk_i32 s2, 0x6000
	v_add_co_u32_e32 v100, vcc, s2, v2
	s_waitcnt vmcnt(23)
	ds_write_b128 v1, v[68:71]
	s_waitcnt vmcnt(22)
	ds_write_b128 v1, v[72:75] offset:1024
	s_waitcnt vmcnt(21)
	ds_write_b128 v1, v[76:79] offset:2048
	s_waitcnt vmcnt(20)
	ds_write_b128 v1, v[80:83] offset:3072
	s_waitcnt vmcnt(19)
	ds_write_b128 v1, v[84:87] offset:4096
	s_waitcnt vmcnt(18)
	ds_write_b128 v1, v[88:91] offset:5120
	s_waitcnt vmcnt(17)
	ds_write_b128 v1, v[92:95] offset:6144
	s_waitcnt vmcnt(16)
	ds_write_b128 v1, v[96:99] offset:7168
	v_addc_co_u32_e32 v101, vcc, 0, v3, vcc
	v_add_co_u32_e32 v104, vcc, s3, v2
	s_waitcnt lgkmcnt(0)
	s_nop 0
	v_addc_co_u32_e32 v105, vcc, 0, v3, vcc
	s_barrier
	global_load_dwordx4 v[68:71], v[104:105], off offset:1024
	global_load_dwordx4 v[72:75], v[104:105], off offset:2048
	global_load_dwordx4 v[76:79], v[104:105], off offset:3072
	global_load_dwordx4 v[80:83], v[102:103], off
	global_load_dwordx4 v[84:87], v[102:103], off offset:1024
	global_load_dwordx4 v[88:91], v[102:103], off offset:2048
	global_load_dwordx4 v[92:95], v[100:101], off offset:-4096
	global_load_dwordx4 v[96:99], v[102:103], off offset:3072
	s_mov_b32 s2, 0x16000
	v_add_co_u32_e32 v102, vcc, s2, v2
	s_mov_b32 s3, 0x17000
	s_nop 0
	v_addc_co_u32_e32 v103, vcc, 0, v3, vcc
	v_add_co_u32_e32 v104, vcc, s3, v2
	s_mov_b32 s3, 0x8000
	s_nop 0
	v_addc_co_u32_e32 v105, vcc, 0, v3, vcc
	s_movk_i32 s2, 0x7000
	v_lshlrev_b32_e32 v134, 4, v0
	s_waitcnt vmcnt(23)
	ds_write_b128 v1, v[4:7] offset:16384
	s_waitcnt vmcnt(22)
	ds_write_b128 v1, v[8:11] offset:17408
	s_waitcnt vmcnt(21)
	ds_write_b128 v1, v[12:15] offset:18432
	s_waitcnt vmcnt(20)
	ds_write_b128 v1, v[16:19] offset:19456
	s_waitcnt vmcnt(19)
	ds_write_b128 v1, v[20:23] offset:20480
	s_waitcnt vmcnt(18)
	ds_write_b128 v1, v[24:27] offset:21504
	s_waitcnt vmcnt(17)
	ds_write_b128 v1, v[28:31] offset:22528
	s_waitcnt vmcnt(16)
	ds_write_b128 v1, v[32:35] offset:23552
	s_waitcnt lgkmcnt(0)
	s_barrier
	global_load_dwordx4 v[4:7], v[100:101], off
	global_load_dwordx4 v[8:11], v[100:101], off offset:1024
	global_load_dwordx4 v[12:15], v[100:101], off offset:2048
	global_load_dwordx4 v[16:19], v[100:101], off offset:3072
	global_load_dwordx4 v[20:23], v[104:105], off offset:-4096
	global_load_dwordx4 v[24:27], v[102:103], off offset:1024
	global_load_dwordx4 v[28:31], v[102:103], off offset:2048
	global_load_dwordx4 v[32:35], v[102:103], off offset:3072
	v_add_co_u32_e32 v100, vcc, s3, v2
	s_waitcnt vmcnt(23)
	ds_write_b128 v1, v[36:39]
	s_waitcnt vmcnt(22)
	ds_write_b128 v1, v[40:43] offset:1024
	s_waitcnt vmcnt(21)
	ds_write_b128 v1, v[44:47] offset:2048
	v_addc_co_u32_e32 v101, vcc, 0, v3, vcc
	v_add_co_u32_e32 v102, vcc, s2, v2
	s_waitcnt vmcnt(20)
	ds_write_b128 v1, v[48:51] offset:3072
	v_addc_co_u32_e32 v103, vcc, 0, v3, vcc
	s_waitcnt vmcnt(19)
	ds_write_b128 v1, v[52:55] offset:4096
	s_waitcnt vmcnt(18)
	ds_write_b128 v1, v[56:59] offset:5120
	s_waitcnt vmcnt(17)
	ds_write_b128 v1, v[60:63] offset:6144
	s_waitcnt vmcnt(16)
	ds_write_b128 v1, v[64:67] offset:7168
	s_waitcnt lgkmcnt(0)
	s_barrier
	global_load_dwordx4 v[36:39], v[100:101], off offset:-4096
	global_load_dwordx4 v[40:43], v[102:103], off offset:1024
	global_load_dwordx4 v[44:47], v[102:103], off offset:2048
	global_load_dwordx4 v[48:51], v[102:103], off offset:3072
	global_load_dwordx4 v[52:55], v[104:105], off
	global_load_dwordx4 v[56:59], v[104:105], off offset:1024
	global_load_dwordx4 v[60:63], v[104:105], off offset:2048
	global_load_dwordx4 v[64:67], v[104:105], off offset:3072
	s_mov_b32 s2, 0x18000
	v_add_co_u32_e32 v102, vcc, s2, v2
	s_mov_b32 s3, 0x19000
	s_nop 0
	v_addc_co_u32_e32 v103, vcc, 0, v3, vcc
	v_add_co_u32_e32 v104, vcc, s3, v2
	s_waitcnt vmcnt(17)
	ds_write_b128 v1, v[92:95] offset:16384
	ds_write_b128 v1, v[68:71] offset:17408
	ds_write_b128 v1, v[72:75] offset:18432
	ds_write_b128 v1, v[76:79] offset:19456
	ds_write_b128 v1, v[80:83] offset:20480
	ds_write_b128 v1, v[84:87] offset:21504
	ds_write_b128 v1, v[88:91] offset:22528
	s_waitcnt vmcnt(16)
	ds_write_b128 v1, v[96:99] offset:23552
	v_addc_co_u32_e32 v105, vcc, 0, v3, vcc
	s_waitcnt lgkmcnt(0)
	s_barrier
	global_load_dwordx4 v[68:71], v[100:101], off
	global_load_dwordx4 v[72:75], v[100:101], off offset:1024
	global_load_dwordx4 v[76:79], v[100:101], off offset:2048
	global_load_dwordx4 v[80:83], v[100:101], off offset:3072
	global_load_dwordx4 v[84:87], v[104:105], off offset:-4096
	global_load_dwordx4 v[88:91], v[102:103], off offset:1024
	global_load_dwordx4 v[92:95], v[102:103], off offset:2048
	s_mov_b32 s3, 0xa000
	v_add_co_u32_e32 v100, vcc, s3, v2
	s_mov_b32 s2, 0x9000
	s_nop 0
	v_addc_co_u32_e32 v101, vcc, 0, v3, vcc
	s_mov_b32 s3, 0xc000
	s_waitcnt vmcnt(22)
	ds_write_b128 v1, v[4:7]
	s_waitcnt vmcnt(21)
	ds_write_b128 v1, v[8:11] offset:1024
	s_waitcnt vmcnt(20)
	ds_write_b128 v1, v[12:15] offset:2048
	global_load_dwordx4 v[4:7], v[102:103], off offset:3072
	s_waitcnt vmcnt(20)
	ds_write_b128 v1, v[16:19] offset:3072
	s_waitcnt vmcnt(19)
	ds_write_b128 v1, v[20:23] offset:4096
	s_waitcnt vmcnt(18)
	ds_write_b128 v1, v[24:27] offset:5120
	s_waitcnt vmcnt(17)
	ds_write_b128 v1, v[28:31] offset:6144
	s_waitcnt vmcnt(16)
	ds_write_b128 v1, v[32:35] offset:7168
	s_waitcnt lgkmcnt(0)
	s_barrier
	global_load_dwordx4 v[8:11], v[100:101], off offset:-4096
	v_add_co_u32_e32 v102, vcc, s2, v2
	s_mov_b32 s2, 0x1a000
	s_nop 0
	v_addc_co_u32_e32 v103, vcc, 0, v3, vcc
	global_load_dwordx4 v[12:15], v[102:103], off offset:1024
	global_load_dwordx4 v[16:19], v[102:103], off offset:2048
	global_load_dwordx4 v[20:23], v[102:103], off offset:3072
	global_load_dwordx4 v[24:27], v[104:105], off
	global_load_dwordx4 v[28:31], v[104:105], off offset:1024
	global_load_dwordx4 v[32:35], v[104:105], off offset:2048
	global_load_dwordx4 v[96:99], v[104:105], off offset:3072
	v_add_co_u32_e32 v102, vcc, s2, v2
	s_mov_b32 s2, 0x1b000
	s_nop 0
	v_addc_co_u32_e32 v103, vcc, 0, v3, vcc
	s_waitcnt vmcnt(23)
	ds_write_b128 v1, v[36:39] offset:16384
	s_waitcnt vmcnt(22)
	ds_write_b128 v1, v[40:43] offset:17408
	s_waitcnt vmcnt(21)
	ds_write_b128 v1, v[44:47] offset:18432
	s_waitcnt vmcnt(20)
	ds_write_b128 v1, v[48:51] offset:19456
	s_waitcnt vmcnt(19)
	ds_write_b128 v1, v[52:55] offset:20480
	s_waitcnt vmcnt(18)
	ds_write_b128 v1, v[56:59] offset:21504
	s_waitcnt vmcnt(17)
	ds_write_b128 v1, v[60:63] offset:22528
	s_waitcnt vmcnt(16)
	ds_write_b128 v1, v[64:67] offset:23552
	s_waitcnt lgkmcnt(0)
	s_barrier
	global_load_dwordx4 v[36:39], v[100:101], off
	global_load_dwordx4 v[40:43], v[100:101], off offset:1024
	global_load_dwordx4 v[44:47], v[100:101], off offset:2048
	v_add_co_u32_e32 v104, vcc, s2, v2
	s_mov_b32 s2, 0xb000
	s_nop 0
	v_addc_co_u32_e32 v105, vcc, 0, v3, vcc
	global_load_dwordx4 v[48:51], v[100:101], off offset:3072
	global_load_dwordx4 v[52:55], v[104:105], off offset:-4096
	global_load_dwordx4 v[56:59], v[102:103], off offset:1024
	global_load_dwordx4 v[60:63], v[102:103], off offset:2048
	global_load_dwordx4 v[64:67], v[102:103], off offset:3072
	s_waitcnt vmcnt(23)
	ds_write_b128 v1, v[68:71]
	s_waitcnt vmcnt(22)
	ds_write_b128 v1, v[72:75] offset:1024
	s_waitcnt vmcnt(21)
	ds_write_b128 v1, v[76:79] offset:2048
	s_waitcnt vmcnt(20)
	ds_write_b128 v1, v[80:83] offset:3072
	s_waitcnt vmcnt(19)
	ds_write_b128 v1, v[84:87] offset:4096
	s_waitcnt vmcnt(18)
	ds_write_b128 v1, v[88:91] offset:5120
	s_waitcnt vmcnt(17)
	ds_write_b128 v1, v[92:95] offset:6144
	s_waitcnt vmcnt(16)
	ds_write_b128 v1, v[4:7] offset:7168
	v_add_co_u32_e32 v84, vcc, s3, v2
	s_waitcnt lgkmcnt(0)
	s_nop 0
	v_addc_co_u32_e32 v85, vcc, 0, v3, vcc
	v_add_co_u32_e32 v80, vcc, s2, v2
	s_barrier
	s_nop 0
	v_addc_co_u32_e32 v81, vcc, 0, v3, vcc
	global_load_dwordx4 v[4:7], v[84:85], off offset:-4096
	global_load_dwordx4 v[68:71], v[80:81], off offset:1024
	global_load_dwordx4 v[72:75], v[80:81], off offset:2048
	s_waitcnt vmcnt(18)
	ds_write_b128 v1, v[8:11] offset:16384
	global_load_dwordx4 v[8:11], v[80:81], off offset:3072
	global_load_dwordx4 v[76:79], v[104:105], off
	s_waitcnt vmcnt(19)
	ds_write_b128 v1, v[12:15] offset:17408
	s_waitcnt vmcnt(18)
	ds_write_b128 v1, v[16:19] offset:18432
	s_mov_b32 s2, 0x1c000
	global_load_dwordx4 v[12:15], v[104:105], off offset:1024
	global_load_dwordx4 v[16:19], v[104:105], off offset:2048
	global_load_dwordx4 v[80:83], v[104:105], off offset:3072
	v_add_co_u32_e32 v88, vcc, s2, v2
	s_mov_b32 s2, 0x1d000
	s_nop 0
	v_addc_co_u32_e32 v89, vcc, 0, v3, vcc
	v_add_co_u32_e32 v100, vcc, s2, v2
	s_mov_b32 s3, 0xe000
	s_nop 0
	v_addc_co_u32_e32 v101, vcc, 0, v3, vcc
	s_waitcnt vmcnt(20)
	ds_write_b128 v1, v[20:23] offset:19456
	s_waitcnt vmcnt(19)
	ds_write_b128 v1, v[24:27] offset:20480
	s_waitcnt vmcnt(18)
	ds_write_b128 v1, v[28:31] offset:21504
	s_waitcnt vmcnt(17)
	ds_write_b128 v1, v[32:35] offset:22528
	s_waitcnt vmcnt(16)
	ds_write_b128 v1, v[96:99] offset:23552
	s_waitcnt lgkmcnt(0)
	s_barrier
	global_load_dwordx4 v[20:23], v[84:85], off
	global_load_dwordx4 v[24:27], v[84:85], off offset:1024
	global_load_dwordx4 v[28:31], v[84:85], off offset:2048
	s_waitcnt vmcnt(18)
	ds_write_b128 v1, v[36:39]
	v_add_co_u32_e32 v102, vcc, s3, v2
	global_load_dwordx4 v[32:35], v[84:85], off offset:3072
	global_load_dwordx4 v[36:39], v[100:101], off offset:-4096
	s_waitcnt vmcnt(19)
	ds_write_b128 v1, v[40:43] offset:1024
	s_waitcnt vmcnt(18)
	ds_write_b128 v1, v[44:47] offset:2048
	s_mov_b32 s2, 0xd000
	v_addc_co_u32_e32 v103, vcc, 0, v3, vcc
	global_load_dwordx4 v[40:43], v[88:89], off offset:1024
	global_load_dwordx4 v[44:47], v[88:89], off offset:2048
	global_load_dwordx4 v[84:87], v[88:89], off offset:3072
	s_waitcnt vmcnt(20)
	ds_write_b128 v1, v[48:51] offset:3072
	s_waitcnt vmcnt(19)
	ds_write_b128 v1, v[52:55] offset:4096
	s_waitcnt vmcnt(18)
	ds_write_b128 v1, v[56:59] offset:5120
	s_waitcnt vmcnt(17)
	ds_write_b128 v1, v[60:63] offset:6144
	s_waitcnt vmcnt(16)
	ds_write_b128 v1, v[64:67] offset:7168
	s_waitcnt lgkmcnt(0)
	s_barrier
	global_load_dwordx4 v[48:51], v[102:103], off offset:-4096
	v_add_co_u32_e32 v104, vcc, s2, v2
	s_mov_b32 s2, 0x1e000
	s_nop 0
	v_addc_co_u32_e32 v105, vcc, 0, v3, vcc
	global_load_dwordx4 v[52:55], v[104:105], off offset:1024
	global_load_dwordx4 v[56:59], v[104:105], off offset:2048
	global_load_dwordx4 v[60:63], v[104:105], off offset:3072
	global_load_dwordx4 v[64:67], v[100:101], off
	global_load_dwordx4 v[88:91], v[100:101], off offset:1024
	global_load_dwordx4 v[92:95], v[100:101], off offset:2048
	global_load_dwordx4 v[96:99], v[100:101], off offset:3072
	v_add_u32_e32 v100, 0xffffff00, v0
	v_ashrrev_i32_e32 v101, 31, v100
	v_lshlrev_b32_e32 v0, 4, v100
	s_waitcnt vmcnt(23)
	ds_write_b128 v1, v[4:7] offset:16384
	s_waitcnt vmcnt(22)
	ds_write_b128 v1, v[68:71] offset:17408
	s_waitcnt vmcnt(21)
	ds_write_b128 v1, v[72:75] offset:18432
	s_waitcnt vmcnt(20)
	ds_write_b128 v1, v[8:11] offset:19456
	s_waitcnt vmcnt(19)
	ds_write_b128 v1, v[76:79] offset:20480
	s_waitcnt vmcnt(18)
	ds_write_b128 v1, v[12:15] offset:21504
	s_waitcnt vmcnt(17)
	ds_write_b128 v1, v[16:19] offset:22528
	s_waitcnt vmcnt(16)
	ds_write_b128 v1, v[80:83] offset:23552
	v_add_co_u32_e32 v68, vcc, s2, v2
	s_mov_b32 s2, 0x1f000
	s_nop 0
	v_addc_co_u32_e32 v69, vcc, 0, v3, vcc
	v_add_co_u32_e32 v76, vcc, s2, v2
	s_waitcnt lgkmcnt(0)
	s_barrier
	global_load_dwordx4 v[4:7], v[102:103], off offset:1024
	global_load_dwordx4 v[8:11], v[102:103], off offset:2048
	v_addc_co_u32_e32 v77, vcc, 0, v3, vcc
	s_waitcnt vmcnt(17)
	ds_write_b128 v1, v[20:23]
	s_mov_b32 s2, 0xf000
	global_load_dwordx4 v[12:15], v[102:103], off offset:3072
	global_load_dwordx4 v[16:19], v[76:77], off offset:-4096
	s_waitcnt vmcnt(18)
	ds_write_b128 v1, v[24:27] offset:1024
	s_waitcnt vmcnt(17)
	ds_write_b128 v1, v[28:31] offset:2048
	v_add_co_u32_e32 v2, vcc, s2, v2
	global_load_dwordx4 v[20:23], v[68:69], off offset:1024
	global_load_dwordx4 v[24:27], v[68:69], off offset:2048
	s_waitcnt vmcnt(18)
	ds_write_b128 v1, v[32:35] offset:3072
	v_addc_co_u32_e32 v3, vcc, 0, v3, vcc
	global_load_dwordx4 v[28:31], v[102:103], off
	global_load_dwordx4 v[32:35], v[68:69], off offset:3072
	s_waitcnt vmcnt(19)
	ds_write_b128 v1, v[36:39] offset:4096
	s_waitcnt vmcnt(18)
	ds_write_b128 v1, v[40:43] offset:5120
	s_waitcnt vmcnt(17)
	ds_write_b128 v1, v[44:47] offset:6144
	s_waitcnt vmcnt(16)
	ds_write_b128 v1, v[84:87] offset:7168
	s_waitcnt lgkmcnt(0)
	s_barrier
	global_load_dwordx4 v[36:39], v[2:3], off
	global_load_dwordx4 v[40:43], v[2:3], off offset:1024
	global_load_dwordx4 v[44:47], v[2:3], off offset:2048
	global_load_dwordx4 v[68:71], v[2:3], off offset:3072
	s_waitcnt vmcnt(19)
	ds_write_b128 v1, v[48:51] offset:16384
	global_load_dwordx4 v[48:51], v[76:77], off
	global_load_dwordx4 v[72:75], v[76:77], off offset:1024
	s_waitcnt vmcnt(20)
	ds_write_b128 v1, v[52:55] offset:17408
	s_waitcnt vmcnt(19)
	ds_write_b128 v1, v[56:59] offset:18432
	v_lshl_add_u64 v[2:3], v[100:101], 4, s[0:1]
	global_load_dwordx4 v[52:55], v[76:77], off offset:2048
	global_load_dwordx4 v[56:59], v[76:77], off offset:3072
	s_waitcnt vmcnt(20)
	ds_write_b128 v1, v[60:63] offset:19456
	s_waitcnt vmcnt(19)
	ds_write_b128 v1, v[64:67] offset:20480
	s_waitcnt vmcnt(18)
	ds_write_b128 v1, v[88:91] offset:21504
	s_waitcnt vmcnt(17)
	ds_write_b128 v1, v[92:95] offset:22528
	s_waitcnt vmcnt(16)
	ds_write_b128 v1, v[96:99] offset:23552
	s_waitcnt lgkmcnt(0)
	s_barrier
	global_load_dwordx4 v[60:63], v[2:3], off
	v_lshl_add_u64 v[2:3], s[0:1], 0, v[134:135]
	v_add_co_u32_e32 v102, vcc, s6, v2
	global_load_dwordx4 v[64:67], v134, s[0:1] offset:-2048
	global_load_dwordx4 v[76:79], v134, s[0:1]
	v_addc_co_u32_e32 v103, vcc, 0, v3, vcc
	v_add_co_u32_e32 v2, vcc, s7, v2
	s_nop 1
	v_addc_co_u32_e32 v3, vcc, 0, v3, vcc
	global_load_dwordx4 v[80:83], v134, s[0:1] offset:2048
	global_load_dwordx4 v[84:87], v[2:3], off offset:-4096
	global_load_dwordx4 v[88:91], v[102:103], off offset:2048
	global_load_dwordx4 v[92:95], v[2:3], off
	global_load_dwordx4 v[96:99], v[2:3], off offset:2048
	s_waitcnt vmcnt(17)
	ds_write_b128 v1, v[28:31]
	ds_write_b128 v1, v[4:7] offset:1024
	ds_write_b128 v1, v[8:11] offset:2048
	ds_write_b128 v1, v[12:15] offset:3072
	ds_write_b128 v1, v[16:19] offset:4096
	ds_write_b128 v1, v[20:23] offset:5120
	ds_write_b128 v1, v[24:27] offset:6144
	s_waitcnt vmcnt(16)
	ds_write_b128 v1, v[32:35] offset:7168
	s_waitcnt lgkmcnt(0)
	s_barrier
	s_waitcnt vmcnt(15)
	ds_write_b128 v1, v[36:39] offset:16384
	s_waitcnt vmcnt(14)
	ds_write_b128 v1, v[40:43] offset:17408
	s_waitcnt vmcnt(13)
	ds_write_b128 v1, v[44:47] offset:18432
	s_waitcnt vmcnt(12)
	ds_write_b128 v1, v[68:71] offset:19456
	s_waitcnt vmcnt(11)
	ds_write_b128 v1, v[48:51] offset:20480
	s_waitcnt vmcnt(10)
	ds_write_b128 v1, v[72:75] offset:21504
	s_waitcnt vmcnt(9)
	ds_write_b128 v1, v[52:55] offset:22528
	s_waitcnt vmcnt(8)
	ds_write_b128 v1, v[56:59] offset:23552
	s_waitcnt lgkmcnt(0)
	s_barrier
	s_waitcnt vmcnt(7)
	ds_write_b128 v0, v[60:63] offset:33792
	s_waitcnt vmcnt(6)
	ds_write_b128 v0, v[64:67] offset:35840
	s_waitcnt vmcnt(5)
	ds_write_b128 v0, v[76:79] offset:37888
	s_waitcnt vmcnt(4)
	ds_write_b128 v0, v[80:83] offset:39936
	s_waitcnt vmcnt(3)
	ds_write_b128 v0, v[84:87] offset:41984
	s_waitcnt vmcnt(2)
	ds_write_b128 v0, v[88:91] offset:44032
	s_waitcnt vmcnt(1)
	ds_write_b128 v0, v[92:95] offset:46080
	s_waitcnt vmcnt(0)
	ds_write_b128 v0, v[96:99] offset:48128
	s_waitcnt lgkmcnt(0)
	s_barrier
	s_endpgm
	s_nop 0
	s_nop 0
	s_nop 0
	s_nop 0
	s_nop 0
	s_nop 0
	s_nop 0
	s_nop 0
	s_nop 0
	s_nop 0
	s_nop 0
	s_nop 0
	s_nop 0
	s_nop 0
	s_nop 0
	s_nop 0
	s_nop 0
	s_nop 0
	s_nop 0
	s_nop 0
	s_nop 0
	s_nop 0
	s_nop 0
	s_nop 0
	s_endpgm
